# layer-3 expert weight conversion moved from setup into idle CUs of the 7 dense GEMM tail rounds (2 items per idle CU)
# speedup vs baseline: 1.0181x; 1.0064x over previous
.LBB0_2:
	v_lshl_add_u32 v1, v0, 2, 0
	v_add_u32_e32 v1, 0x20000, v1
	v_mov_b32_e32 v2, 0
	ds_write2st64_b32 v1, v2, v2 offset1:8
	ds_write2st64_b32 v1, v2, v2 offset0:16 offset1:24
	v_or_b32_e32 v1, 0x800, v0
	s_mov_b64 s[0:1], -1
	s_and_saveexec_b64 s[2:3], s[0:1]
	v_lshl_add_u32 v3, v1, 2, 0
	v_add_u32_e32 v3, 0x20000, v3
	ds_write_b32 v3, v2
	s_or_b64 exec, exec, s[2:3]
	s_and_saveexec_b64 s[2:3], s[0:1]
	s_add_i32 s0, 0, 0x20000
	v_lshl_add_u32 v1, v1, 2, s0
	v_mov_b32_e32 v2, 0
	ds_write_b32 v1, v2 offset:2048
	s_or_b64 exec, exec, s[2:3]
	v_readlane_b32 s0, v254, 0
	v_readlane_b32 s1, v254, 1
	s_load_dwordx2 s[88:89], s[0:1], 0xd0
	v_or_b32_e32 v1, 0xc00, v0
	v_cmp_gt_u32_e64 s[0:1], 7, 6
	v_cmp_gt_u32_e64 s[4:5], 7, 5
	s_and_saveexec_b64 s[2:3], s[4:5]
	v_lshl_add_u32 v2, v1, 2, 0
	v_add_u32_e32 v2, 0x20000, v2
	v_mov_b32_e32 v3, 0
	ds_write_b32 v2, v3
	s_or_b64 exec, exec, s[2:3]
	s_and_saveexec_b64 s[2:3], s[0:1]
	s_add_i32 s0, 0, 0x20000
	v_lshl_add_u32 v1, v1, 2, s0
	v_mov_b32_e32 v2, 0
	ds_write_b32 v1, v2 offset:2048
	s_or_b64 exec, exec, s[2:3]
	s_waitcnt lgkmcnt(0)
	s_barrier
	s_mov_b32 s99, 0
	s_add_u32 s92, s88, 0x4000
	s_getreg_b32 s0, hwreg(HW_REG_XCC_ID, 0, 4)
	s_addc_u32 s93, s89, 0
	s_and_b32 s0, s0, 15
	v_writelane_b32 v254, s0, 6
	v_cmp_eq_u32_e32 vcc, 0, v0
	s_and_saveexec_b64 s[0:1], vcc
	s_cbranch_execz .LBB0_13
	s_mov_b64 s[2:3], exec
	v_mbcnt_lo_u32_b32 v0, s2, 0
	v_mbcnt_hi_u32_b32 v0, s3, v0
	v_cmp_eq_u32_e32 vcc, 0, v0
	s_and_b64 s[4:5], exec, vcc
	s_mov_b64 exec, s[4:5]
	s_cbranch_execz .LBB0_13
	v_readlane_b32 s4, v254, 6
	s_lshl_b32 s4, s4, 8
	s_bcnt1_i32_b64 s2, s[2:3]
	v_mov_b32_e32 v0, s4
	v_mov_b32_e32 v1, s2
	global_atomic_add v0, v1, s[92:93] offset:1024

.LBB0_55:
	s_cmp_lg_u32 s99, 0
	s_cbranch_scc1 .Ltc_itemdone
	v_readlane_b32 s2, v254, 0
	v_readlane_b32 s3, v254, 1
	s_load_dword s0, s[2:3], 0xe8
	s_add_i32 s14, s14, s15
	s_add_i32 s16, s16, s17
	s_add_i32 s10, s10, s18
	s_waitcnt lgkmcnt(0)
	s_add_i32 s22, s22, s0
	s_cmp_lt_i32 s22, 0x1800
	s_cbranch_scc1 .Ltc_noskip
	s_cmp_ge_i32 s22, 0x2000
	s_cbranch_scc1 .Ltc_noskip
	s_addk_i32 s22, 0x800
	s_add_i32 s14, s14, 0x10000
	s_add_i32 s16, s16, 0x8000
	s_add_i32 s10, s10, 0x100000
.Ltc_noskip:
	s_cmpk_lt_i32 s22, 0x2c00
	s_cbranch_scc0 .LBB0_60

.Ltc_next:
	s_cmp_ge_u32 s100, 0xc00
	s_cbranch_scc1 .Ltc_alldone
	s_movk_i32 s0, 0x2400
	s_cmp_lt_u32 s100, 0x800
	s_cselect_b32 s22, 0x1800, s0
	s_add_i32 s22, s22, s100
	v_mbcnt_lo_u32_b32 v0, -1, 0
	v_mbcnt_hi_u32_b32 v0, -1, v0
	s_and_b32 s0, s94, 0xffffffc0
	s_nop 0
	v_ashrrev_i32_e32 v1, 31, v0
	v_add_u32_e32 v2, s0, v0
	s_movk_i32 s0, 0x44
	v_lshlrev_b32_e32 v5, 7, v0
	v_mul_lo_u32 v4, v0, s0
	v_mul_lo_u32 v12, v2, s0
	v_lshrrev_b32_e32 v3, 1, v2
	v_and_b32_e32 v5, 0x80, v5
	s_movk_i32 s0, 0x7f
	v_and_or_b32 v3, v3, s0, v5
	s_lshl_b32 s6, s95, 3
	s_add_u32 s7, s88, 0x22000000
	s_addc_u32 s11, s89, 0
	v_add_u32_e32 v4, 0, v4
	s_add_u32 s12, s88, 0x2000000
	v_add_u32_e32 v4, s6, v4
	s_mov_b32 s1, 0
	s_addc_u32 s13, s89, 0
	s_lshl_b32 s14, s22, 5
	s_lshl_b32 s16, s22, 4
	s_lshl_b32 s10, s22, 9
	s_mov_b32 s19, 0xc3e00000
	s_movk_i32 s20, 0xff
	v_add_u32_e32 v5, 0x1100, v4
	v_add_u32_e32 v6, 0x2200, v4
	v_add_u32_e32 v7, 0x3300, v4
	v_add_u32_e32 v8, 0x4400, v4
	v_add_u32_e32 v9, 0x5500, v4
	v_add_u32_e32 v10, 0x6600, v4
	v_add_u32_e32 v11, 0x7700, v4
	v_add_u32_e32 v12, 0, v12
	s_movk_i32 s21, 0xff00
	v_mov_b32_e32 v13, 0x43e00000
	v_mov_b32_e32 v14, 8
	s_branch .LBB0_56
.Ltc_itemdone:
	s_add_i32 s100, s100, s101
	s_sub_u32 s98, s98, 1
	s_cmp_lg_u32 s98, 0
	s_cbranch_scc1 .Ltc_next
.Ltc_alldone:
	s_cmp_eq_u32 s99, 1
	s_cbranch_scc1 .Ltc_ret_1
	s_cmp_eq_u32 s99, 2
	s_cbranch_scc1 .Ltc_ret_2
	s_cmp_eq_u32 s99, 3
	s_cbranch_scc1 .Ltc_ret_3
	s_cmp_eq_u32 s99, 4
	s_cbranch_scc1 .Ltc_ret_4
	s_branch .Ltc_s1_fwd

.LBB0_197:
	s_cmp_lt_u32 s96, 32
	s_cbranch_scc1 .Ltc_skip_1
	v_writelane_b32 v200, s0, 0
	s_nop 1
	v_writelane_b32 v200, s1, 1
	s_nop 1
	v_writelane_b32 v200, s2, 2
	s_nop 1
	v_writelane_b32 v200, s3, 3
	s_nop 1
	v_writelane_b32 v200, s4, 4
	s_nop 1
	v_writelane_b32 v200, s5, 5
	s_nop 1
	v_writelane_b32 v200, s6, 6
	s_nop 1
	v_writelane_b32 v200, s7, 7
	s_nop 1
	v_writelane_b32 v200, s10, 8
	s_nop 1
	v_writelane_b32 v200, s11, 9
	s_nop 1
	v_writelane_b32 v200, s12, 10
	s_nop 1
	v_writelane_b32 v200, s13, 11
	s_nop 1
	v_writelane_b32 v200, s14, 12
	s_nop 1
	v_writelane_b32 v200, s15, 13
	s_nop 1
	v_writelane_b32 v200, s16, 14
	s_nop 1
	v_writelane_b32 v200, s17, 15
	s_nop 1
	v_writelane_b32 v200, s18, 16
	s_nop 1
	v_writelane_b32 v200, s19, 17
	s_nop 1
	v_writelane_b32 v200, s20, 18
	s_nop 1
	v_writelane_b32 v200, s21, 19
	s_nop 1
	v_writelane_b32 v200, s22, 20
	s_nop 1
	v_writelane_b32 v200, s23, 21
	s_nop 1
	v_writelane_b32 v200, s24, 22
	s_nop 1
	v_writelane_b32 v200, s25, 23
	s_nop 1
	v_writelane_b32 v200, s36, 24
	s_nop 1
	v_writelane_b32 v200, s37, 25
	s_nop 1
	v_writelane_b32 v200, s38, 26
	s_nop 1
	v_writelane_b32 v200, s39, 27
	s_nop 1
	v_writelane_b32 v200, s40, 28
	s_nop 1
	v_writelane_b32 v200, s41, 29
	s_nop 1
	v_writelane_b32 v200, s42, 30
	s_nop 1
	v_writelane_b32 v200, s43, 31
	s_nop 1
	v_writelane_b32 v200, s44, 32
	s_nop 1
	v_writelane_b32 v200, s45, 33
	s_nop 1
	v_writelane_b32 v200, s46, 34
	s_nop 1
	v_writelane_b32 v200, s47, 35
	s_nop 1
	v_writelane_b32 v200, s48, 36
	s_nop 1
	v_writelane_b32 v200, s49, 37
	s_nop 1
	v_writelane_b32 v200, s50, 38
	s_nop 1
	v_writelane_b32 v200, s51, 39
	s_nop 1
	s_mov_b32 s99, 1
	s_mov_b32 s98, 2
	s_mov_b32 s101, 224
	s_sub_i32 s100, s96, 32
	s_branch .Ltc_next
.Ltc_ret_1:
	s_mov_b32 s99, 0
	v_readlane_b32 s0, v200, 0
	v_readlane_b32 s1, v200, 1
	v_readlane_b32 s2, v200, 2
	v_readlane_b32 s3, v200, 3
	v_readlane_b32 s4, v200, 4
	v_readlane_b32 s5, v200, 5
	v_readlane_b32 s6, v200, 6
	v_readlane_b32 s7, v200, 7
	v_readlane_b32 s10, v200, 8
	v_readlane_b32 s11, v200, 9
	v_readlane_b32 s12, v200, 10
	v_readlane_b32 s13, v200, 11
	v_readlane_b32 s14, v200, 12
	v_readlane_b32 s15, v200, 13
	v_readlane_b32 s16, v200, 14
	v_readlane_b32 s17, v200, 15
	v_readlane_b32 s18, v200, 16
	v_readlane_b32 s19, v200, 17
	v_readlane_b32 s20, v200, 18
	v_readlane_b32 s21, v200, 19
	v_readlane_b32 s22, v200, 20
	v_readlane_b32 s23, v200, 21
	v_readlane_b32 s24, v200, 22
	v_readlane_b32 s25, v200, 23
	v_readlane_b32 s36, v200, 24
	v_readlane_b32 s37, v200, 25
	v_readlane_b32 s38, v200, 26
	v_readlane_b32 s39, v200, 27
	v_readlane_b32 s40, v200, 28
	v_readlane_b32 s41, v200, 29
	v_readlane_b32 s42, v200, 30
	v_readlane_b32 s43, v200, 31
	v_readlane_b32 s44, v200, 32
	v_readlane_b32 s45, v200, 33
	v_readlane_b32 s46, v200, 34
	v_readlane_b32 s47, v200, 35
	v_readlane_b32 s48, v200, 36
	v_readlane_b32 s49, v200, 37
	v_readlane_b32 s50, v200, 38
	v_readlane_b32 s51, v200, 39
	s_nop 1

.LBB0_359:
	s_cmp_lt_u32 s96, 32
	s_cbranch_scc1 .Ltc_skip_2
	v_writelane_b32 v200, s0, 0
	s_nop 1
	v_writelane_b32 v200, s1, 1
	s_nop 1
	v_writelane_b32 v200, s2, 2
	s_nop 1
	v_writelane_b32 v200, s3, 3
	s_nop 1
	v_writelane_b32 v200, s4, 4
	s_nop 1
	v_writelane_b32 v200, s5, 5
	s_nop 1
	v_writelane_b32 v200, s6, 6
	s_nop 1
	v_writelane_b32 v200, s7, 7
	s_nop 1
	v_writelane_b32 v200, s10, 8
	s_nop 1
	v_writelane_b32 v200, s11, 9
	s_nop 1
	v_writelane_b32 v200, s12, 10
	s_nop 1
	v_writelane_b32 v200, s13, 11
	s_nop 1
	v_writelane_b32 v200, s14, 12
	s_nop 1
	v_writelane_b32 v200, s15, 13
	s_nop 1
	v_writelane_b32 v200, s16, 14
	s_nop 1
	v_writelane_b32 v200, s17, 15
	s_nop 1
	v_writelane_b32 v200, s18, 16
	s_nop 1
	v_writelane_b32 v200, s19, 17
	s_nop 1
	v_writelane_b32 v200, s20, 18
	s_nop 1
	v_writelane_b32 v200, s21, 19
	s_nop 1
	v_writelane_b32 v200, s22, 20
	s_nop 1
	v_writelane_b32 v200, s23, 21
	s_nop 1
	v_writelane_b32 v200, s24, 22
	s_nop 1
	v_writelane_b32 v200, s25, 23
	s_nop 1
	v_writelane_b32 v200, s36, 24
	s_nop 1
	v_writelane_b32 v200, s37, 25
	s_nop 1
	v_writelane_b32 v200, s38, 26
	s_nop 1
	v_writelane_b32 v200, s39, 27
	s_nop 1
	v_writelane_b32 v200, s40, 28
	s_nop 1
	v_writelane_b32 v200, s41, 29
	s_nop 1
	v_writelane_b32 v200, s42, 30
	s_nop 1
	v_writelane_b32 v200, s43, 31
	s_nop 1
	v_writelane_b32 v200, s44, 32
	s_nop 1
	v_writelane_b32 v200, s45, 33
	s_nop 1
	v_writelane_b32 v200, s46, 34
	s_nop 1
	v_writelane_b32 v200, s47, 35
	s_nop 1
	v_writelane_b32 v200, s48, 36
	s_nop 1
	v_writelane_b32 v200, s49, 37
	s_nop 1
	v_writelane_b32 v200, s50, 38
	s_nop 1
	v_writelane_b32 v200, s51, 39
	s_nop 1
	s_mov_b32 s99, 2
	s_mov_b32 s98, 2
	s_mov_b32 s101, 224
	s_add_i32 s100, s96, 416
	s_branch .Ltc_next

.LBB0_807:
	s_cmp_lt_u32 s96, 48
	s_cbranch_scc1 .Ltc_skip_3
	v_writelane_b32 v200, s0, 0
	s_nop 1
	v_writelane_b32 v200, s1, 1
	s_nop 1
	v_writelane_b32 v200, s2, 2
	s_nop 1
	v_writelane_b32 v200, s3, 3
	s_nop 1
	v_writelane_b32 v200, s4, 4
	s_nop 1
	v_writelane_b32 v200, s5, 5
	s_nop 1
	v_writelane_b32 v200, s6, 6
	s_nop 1
	v_writelane_b32 v200, s7, 7
	s_nop 1
	v_writelane_b32 v200, s10, 8
	s_nop 1
	v_writelane_b32 v200, s11, 9
	s_nop 1
	v_writelane_b32 v200, s12, 10
	s_nop 1
	v_writelane_b32 v200, s13, 11
	s_nop 1
	v_writelane_b32 v200, s14, 12
	s_nop 1
	v_writelane_b32 v200, s15, 13
	s_nop 1
	v_writelane_b32 v200, s16, 14
	s_nop 1
	v_writelane_b32 v200, s17, 15
	s_nop 1
	v_writelane_b32 v200, s18, 16
	s_nop 1
	v_writelane_b32 v200, s19, 17
	s_nop 1
	v_writelane_b32 v200, s20, 18
	s_nop 1
	v_writelane_b32 v200, s21, 19
	s_nop 1
	v_writelane_b32 v200, s22, 20
	s_nop 1
	v_writelane_b32 v200, s23, 21
	s_nop 1
	v_writelane_b32 v200, s24, 22
	s_nop 1
	v_writelane_b32 v200, s25, 23
	s_nop 1
	v_writelane_b32 v200, s36, 24
	s_nop 1
	v_writelane_b32 v200, s37, 25
	s_nop 1
	v_writelane_b32 v200, s38, 26
	s_nop 1
	v_writelane_b32 v200, s39, 27
	s_nop 1
	v_writelane_b32 v200, s40, 28
	s_nop 1
	v_writelane_b32 v200, s41, 29
	s_nop 1
	v_writelane_b32 v200, s42, 30
	s_nop 1
	v_writelane_b32 v200, s43, 31
	s_nop 1
	v_writelane_b32 v200, s44, 32
	s_nop 1
	v_writelane_b32 v200, s45, 33
	s_nop 1
	v_writelane_b32 v200, s46, 34
	s_nop 1
	v_writelane_b32 v200, s47, 35
	s_nop 1
	v_writelane_b32 v200, s48, 36
	s_nop 1
	v_writelane_b32 v200, s49, 37
	s_nop 1
	v_writelane_b32 v200, s50, 38
	s_nop 1
	v_writelane_b32 v200, s51, 39
	s_nop 1
	s_mov_b32 s99, 3
	s_mov_b32 s98, 2
	s_mov_b32 s101, 208
	s_add_i32 s100, s96, 848
	s_branch .Ltc_next

.Ltc_s1_back:
	s_branch .Ltc_next
.Ltc_s1_fwd:
	s_cmp_eq_u32 s99, 5
	s_cbranch_scc1 .Ltc_ret_5
	s_cmp_eq_u32 s99, 6
	s_cbranch_scc1 .Ltc_ret_6
	s_branch .Ltc_s2_fwd

.LBB0_1052:
	s_cmp_lt_u32 s96, 32
	s_cbranch_scc1 .Ltc_skip_4
	v_writelane_b32 v200, s0, 0
	s_nop 1
	v_writelane_b32 v200, s1, 1
	s_nop 1
	v_writelane_b32 v200, s2, 2
	s_nop 1
	v_writelane_b32 v200, s3, 3
	s_nop 1
	v_writelane_b32 v200, s4, 4
	s_nop 1
	v_writelane_b32 v200, s5, 5
	s_nop 1
	v_writelane_b32 v200, s6, 6
	s_nop 1
	v_writelane_b32 v200, s7, 7
	s_nop 1
	v_writelane_b32 v200, s10, 8
	s_nop 1
	v_writelane_b32 v200, s11, 9
	s_nop 1
	v_writelane_b32 v200, s12, 10
	s_nop 1
	v_writelane_b32 v200, s13, 11
	s_nop 1
	v_writelane_b32 v200, s14, 12
	s_nop 1
	v_writelane_b32 v200, s15, 13
	s_nop 1
	v_writelane_b32 v200, s16, 14
	s_nop 1
	v_writelane_b32 v200, s17, 15
	s_nop 1
	v_writelane_b32 v200, s18, 16
	s_nop 1
	v_writelane_b32 v200, s19, 17
	s_nop 1
	v_writelane_b32 v200, s20, 18
	s_nop 1
	v_writelane_b32 v200, s21, 19
	s_nop 1
	v_writelane_b32 v200, s22, 20
	s_nop 1
	v_writelane_b32 v200, s23, 21
	s_nop 1
	v_writelane_b32 v200, s24, 22
	s_nop 1
	v_writelane_b32 v200, s25, 23
	s_nop 1
	v_writelane_b32 v200, s36, 24
	s_nop 1
	v_writelane_b32 v200, s37, 25
	s_nop 1
	v_writelane_b32 v200, s38, 26
	s_nop 1
	v_writelane_b32 v200, s39, 27
	s_nop 1
	v_writelane_b32 v200, s40, 28
	s_nop 1
	v_writelane_b32 v200, s41, 29
	s_nop 1
	v_writelane_b32 v200, s42, 30
	s_nop 1
	v_writelane_b32 v200, s43, 31
	s_nop 1
	v_writelane_b32 v200, s44, 32
	s_nop 1
	v_writelane_b32 v200, s45, 33
	s_nop 1
	v_writelane_b32 v200, s46, 34
	s_nop 1
	v_writelane_b32 v200, s47, 35
	s_nop 1
	v_writelane_b32 v200, s48, 36
	s_nop 1
	v_writelane_b32 v200, s49, 37
	s_nop 1
	v_writelane_b32 v200, s50, 38
	s_nop 1
	v_writelane_b32 v200, s51, 39
	s_nop 1
	s_mov_b32 s99, 4
	s_mov_b32 s98, 2
	s_mov_b32 s101, 224
	s_add_i32 s100, s96, 1280
	s_branch .Ltc_next

.LBB0_1495:
	s_cmp_lt_u32 s96, 48
	s_cbranch_scc1 .Ltc_skip_5
	v_writelane_b32 v200, s0, 0
	s_nop 1
	v_writelane_b32 v200, s1, 1
	s_nop 1
	v_writelane_b32 v200, s2, 2
	s_nop 1
	v_writelane_b32 v200, s3, 3
	s_nop 1
	v_writelane_b32 v200, s4, 4
	s_nop 1
	v_writelane_b32 v200, s5, 5
	s_nop 1
	v_writelane_b32 v200, s6, 6
	s_nop 1
	v_writelane_b32 v200, s7, 7
	s_nop 1
	v_writelane_b32 v200, s10, 8
	s_nop 1
	v_writelane_b32 v200, s11, 9
	s_nop 1
	v_writelane_b32 v200, s12, 10
	s_nop 1
	v_writelane_b32 v200, s13, 11
	s_nop 1
	v_writelane_b32 v200, s14, 12
	s_nop 1
	v_writelane_b32 v200, s15, 13
	s_nop 1
	v_writelane_b32 v200, s16, 14
	s_nop 1
	v_writelane_b32 v200, s17, 15
	s_nop 1
	v_writelane_b32 v200, s18, 16
	s_nop 1
	v_writelane_b32 v200, s19, 17
	s_nop 1
	v_writelane_b32 v200, s20, 18
	s_nop 1
	v_writelane_b32 v200, s21, 19
	s_nop 1
	v_writelane_b32 v200, s22, 20
	s_nop 1
	v_writelane_b32 v200, s23, 21
	s_nop 1
	v_writelane_b32 v200, s24, 22
	s_nop 1
	v_writelane_b32 v200, s25, 23
	s_nop 1
	v_writelane_b32 v200, s36, 24
	s_nop 1
	v_writelane_b32 v200, s37, 25
	s_nop 1
	v_writelane_b32 v200, s38, 26
	s_nop 1
	v_writelane_b32 v200, s39, 27
	s_nop 1
	v_writelane_b32 v200, s40, 28
	s_nop 1
	v_writelane_b32 v200, s41, 29
	s_nop 1
	v_writelane_b32 v200, s42, 30
	s_nop 1
	v_writelane_b32 v200, s43, 31
	s_nop 1
	v_writelane_b32 v200, s44, 32
	s_nop 1
	v_writelane_b32 v200, s45, 33
	s_nop 1
	v_writelane_b32 v200, s46, 34
	s_nop 1
	v_writelane_b32 v200, s47, 35
	s_nop 1
	v_writelane_b32 v200, s48, 36
	s_nop 1
	v_writelane_b32 v200, s49, 37
	s_nop 1
	v_writelane_b32 v200, s50, 38
	s_nop 1
	v_writelane_b32 v200, s51, 39
	s_nop 1
	s_mov_b32 s99, 5
	s_mov_b32 s98, 2
	s_mov_b32 s101, 208
	s_add_i32 s100, s96, 1712
	s_branch .Ltc_s1_back

.LBB0_1711:
	s_cmp_lt_u32 s96, 32
	s_cbranch_scc1 .Ltc_skip_6
	v_writelane_b32 v200, s0, 0
	s_nop 1
	v_writelane_b32 v200, s1, 1
	s_nop 1
	v_writelane_b32 v200, s2, 2
	s_nop 1
	v_writelane_b32 v200, s3, 3
	s_nop 1
	v_writelane_b32 v200, s4, 4
	s_nop 1
	v_writelane_b32 v200, s5, 5
	s_nop 1
	v_writelane_b32 v200, s6, 6
	s_nop 1
	v_writelane_b32 v200, s7, 7
	s_nop 1
	v_writelane_b32 v200, s10, 8
	s_nop 1
	v_writelane_b32 v200, s11, 9
	s_nop 1
	v_writelane_b32 v200, s12, 10
	s_nop 1
	v_writelane_b32 v200, s13, 11
	s_nop 1
	v_writelane_b32 v200, s14, 12
	s_nop 1
	v_writelane_b32 v200, s15, 13
	s_nop 1
	v_writelane_b32 v200, s16, 14
	s_nop 1
	v_writelane_b32 v200, s17, 15
	s_nop 1
	v_writelane_b32 v200, s18, 16
	s_nop 1
	v_writelane_b32 v200, s19, 17
	s_nop 1
	v_writelane_b32 v200, s20, 18
	s_nop 1
	v_writelane_b32 v200, s21, 19
	s_nop 1
	v_writelane_b32 v200, s22, 20
	s_nop 1
	v_writelane_b32 v200, s23, 21
	s_nop 1
	v_writelane_b32 v200, s24, 22
	s_nop 1
	v_writelane_b32 v200, s25, 23
	s_nop 1
	v_writelane_b32 v200, s36, 24
	s_nop 1
	v_writelane_b32 v200, s37, 25
	s_nop 1
	v_writelane_b32 v200, s38, 26
	s_nop 1
	v_writelane_b32 v200, s39, 27
	s_nop 1
	v_writelane_b32 v200, s40, 28
	s_nop 1
	v_writelane_b32 v200, s41, 29
	s_nop 1
	v_writelane_b32 v200, s42, 30
	s_nop 1
	v_writelane_b32 v200, s43, 31
	s_nop 1
	v_writelane_b32 v200, s44, 32
	s_nop 1
	v_writelane_b32 v200, s45, 33
	s_nop 1
	v_writelane_b32 v200, s46, 34
	s_nop 1
	v_writelane_b32 v200, s47, 35
	s_nop 1
	v_writelane_b32 v200, s48, 36
	s_nop 1
	v_writelane_b32 v200, s49, 37
	s_nop 1
	v_writelane_b32 v200, s50, 38
	s_nop 1
	v_writelane_b32 v200, s51, 39
	s_nop 1
	s_mov_b32 s99, 6
	s_mov_b32 s98, 2
	s_mov_b32 s101, 224
	s_add_i32 s100, s96, 2144
	s_branch .Ltc_s1_back

.LBB0_2154:
	s_cmp_lt_u32 s96, 32
	s_cbranch_scc1 .Ltc_skip_7
	v_writelane_b32 v200, s0, 0
	s_nop 1
	v_writelane_b32 v200, s1, 1
	s_nop 1
	v_writelane_b32 v200, s2, 2
	s_nop 1
	v_writelane_b32 v200, s3, 3
	s_nop 1
	v_writelane_b32 v200, s4, 4
	s_nop 1
	v_writelane_b32 v200, s5, 5
	s_nop 1
	v_writelane_b32 v200, s6, 6
	s_nop 1
	v_writelane_b32 v200, s7, 7
	s_nop 1
	v_writelane_b32 v200, s10, 8
	s_nop 1
	v_writelane_b32 v200, s11, 9
	s_nop 1
	v_writelane_b32 v200, s12, 10
	s_nop 1
	v_writelane_b32 v200, s13, 11
	s_nop 1
	v_writelane_b32 v200, s14, 12
	s_nop 1
	v_writelane_b32 v200, s15, 13
	s_nop 1
	v_writelane_b32 v200, s16, 14
	s_nop 1
	v_writelane_b32 v200, s17, 15
	s_nop 1
	v_writelane_b32 v200, s18, 16
	s_nop 1
	v_writelane_b32 v200, s19, 17
	s_nop 1
	v_writelane_b32 v200, s20, 18
	s_nop 1
	v_writelane_b32 v200, s21, 19
	s_nop 1
	v_writelane_b32 v200, s22, 20
	s_nop 1
	v_writelane_b32 v200, s23, 21
	s_nop 1
	v_writelane_b32 v200, s24, 22
	s_nop 1
	v_writelane_b32 v200, s25, 23
	s_nop 1
	v_writelane_b32 v200, s36, 24
	s_nop 1
	v_writelane_b32 v200, s37, 25
	s_nop 1
	v_writelane_b32 v200, s38, 26
	s_nop 1
	v_writelane_b32 v200, s39, 27
	s_nop 1
	v_writelane_b32 v200, s40, 28
	s_nop 1
	v_writelane_b32 v200, s41, 29
	s_nop 1
	v_writelane_b32 v200, s42, 30
	s_nop 1
	v_writelane_b32 v200, s43, 31
	s_nop 1
	v_writelane_b32 v200, s44, 32
	s_nop 1
	v_writelane_b32 v200, s45, 33
	s_nop 1
	v_writelane_b32 v200, s46, 34
	s_nop 1
	v_writelane_b32 v200, s47, 35
	s_nop 1
	v_writelane_b32 v200, s48, 36
	s_nop 1
	v_writelane_b32 v200, s49, 37
	s_nop 1
	v_writelane_b32 v200, s50, 38
	s_nop 1
	v_writelane_b32 v200, s51, 39
	s_nop 1
	s_mov_b32 s99, 7
	s_mov_b32 s98, 2
	s_mov_b32 s101, 224
	s_add_i32 s100, s96, 2592
	s_branch .Ltc_s2_back

	.amdhsa_kernel _Z3fwd4Args
		.amdhsa_group_segment_fixed_size 0
		.amdhsa_private_segment_fixed_size 0
		.amdhsa_kernarg_size 488
		.amdhsa_user_sgpr_count 2
		.amdhsa_user_sgpr_dispatch_ptr 0
		.amdhsa_user_sgpr_queue_ptr 0
		.amdhsa_user_sgpr_kernarg_segment_ptr 1
		.amdhsa_user_sgpr_dispatch_id 0
		.amdhsa_user_sgpr_kernarg_preload_length 0
		.amdhsa_user_sgpr_kernarg_preload_offset 0
		.amdhsa_user_sgpr_private_segment_size 0
		.amdhsa_uses_dynamic_stack 0
		.amdhsa_enable_private_segment 0
		.amdhsa_system_sgpr_workgroup_id_x 1
		.amdhsa_system_sgpr_workgroup_id_y 0
		.amdhsa_system_sgpr_workgroup_id_z 0
		.amdhsa_system_sgpr_workgroup_info 0
		.amdhsa_system_vgpr_workitem_id 0
		.amdhsa_next_free_vgpr 256
		.amdhsa_next_free_sgpr 102
		.amdhsa_accum_offset 256
		.amdhsa_reserve_vcc 1
		.amdhsa_float_round_mode_32 0
		.amdhsa_float_round_mode_16_64 0
		.amdhsa_float_denorm_mode_32 3
		.amdhsa_float_denorm_mode_16_64 3
		.amdhsa_dx10_clamp 1
		.amdhsa_ieee_mode 1
		.amdhsa_fp16_overflow 0
		.amdhsa_tg_split 0
		.amdhsa_exception_fp_ieee_invalid_op 0
		.amdhsa_exception_fp_denorm_src 0
		.amdhsa_exception_fp_ieee_div_zero 0
		.amdhsa_exception_fp_ieee_overflow 0
		.amdhsa_exception_fp_ieee_underflow 0
		.amdhsa_exception_fp_ieee_inexact 0
		.amdhsa_exception_int_div_zero 0
	.end_amdhsa_kernel

amdhsa.kernels:
  - .agpr_count:     0
    .args:
      - .offset:         0
        .size:           232
        .value_kind:     by_value
      - .offset:         232
        .size:           4
        .value_kind:     hidden_block_count_x
      - .offset:         236
        .size:           4
        .value_kind:     hidden_block_count_y
      - .offset:         240
        .size:           4
        .value_kind:     hidden_block_count_z
      - .offset:         244
        .size:           2
        .value_kind:     hidden_group_size_x
      - .offset:         246
        .size:           2
        .value_kind:     hidden_group_size_y
      - .offset:         248
        .size:           2
        .value_kind:     hidden_group_size_z
      - .offset:         250
        .size:           2
        .value_kind:     hidden_remainder_x
      - .offset:         252
        .size:           2
        .value_kind:     hidden_remainder_y
      - .offset:         254
        .size:           2
        .value_kind:     hidden_remainder_z
      - .offset:         272
        .size:           8
        .value_kind:     hidden_global_offset_x
      - .offset:         280
        .size:           8
        .value_kind:     hidden_global_offset_y
      - .offset:         288
        .size:           8
        .value_kind:     hidden_global_offset_z
      - .offset:         296
        .size:           2
        .value_kind:     hidden_grid_dims
      - .offset:         352
        .size:           4
        .value_kind:     hidden_dynamic_lds_size
    .group_segment_fixed_size: 0
    .kernarg_segment_align: 8
    .kernarg_segment_size: 488
    .language:       OpenCL C
    .language_version:
      - 2
      - 0
    .max_flat_workgroup_size: 512
    .name:           _Z3fwd4Args
    .private_segment_fixed_size: 0
    .sgpr_count:     108
    .sgpr_spill_count: 117
    .symbol:         _Z3fwd4Args.kd
    .uniform_work_group_size: 1
    .uses_dynamic_stack: false
    .vgpr_count:     256
    .vgpr_spill_count: 0
    .wavefront_size: 64
